# baseline (speedup 1.0000x reference)
.LBB0_338:
	global_load_dword v181, v[118:119], off
	v_lshl_add_u64 v[190:191], s[92:93], 0, v[116:117]
	global_load_dwordx2 v[66:67], v[190:191], off offset:-128
	global_load_dwordx2 v[68:69], v[190:191], off offset:-64
	global_load_dwordx2 v[138:139], v[190:191], off offset:-32
	global_load_dwordx2 v[136:137], v[190:191], off
	global_load_dwordx2 v[134:135], v[190:191], off offset:32
	global_load_dwordx2 v[132:133], v[190:191], off offset:64
	global_load_dwordx2 v[130:131], v[190:191], off offset:96
	ds_read_b128 v[62:65], v160
	ds_read_b128 v[58:61], v161
	ds_read_b128 v[54:57], v162
	ds_read_b128 v[50:53], v163
	ds_read_b64_tr_b16 v[192:193], v164 offset:32768
	ds_read_b64_tr_b16 v[194:195], v165 offset:33792
	ds_read_b64_tr_b16 v[196:197], v164 offset:40960
	ds_read_b64_tr_b16 v[198:199], v165 offset:41984
	ds_read_b64_tr_b16 v[200:201], v164 offset:49152
	ds_read_b64_tr_b16 v[202:203], v165 offset:50176
	ds_read_b64_tr_b16 v[204:205], v164 offset:57344
	ds_read_b64_tr_b16 v[206:207], v165 offset:58368
	ds_read_b64_tr_b16 v[208:209], v166 offset:32768
	ds_read_b64_tr_b16 v[210:211], v167 offset:33792
	ds_read_b64_tr_b16 v[212:213], v166 offset:40960
	ds_read_b64_tr_b16 v[214:215], v167 offset:41984
	ds_read_b64_tr_b16 v[216:217], v166 offset:49152
	ds_read_b64_tr_b16 v[218:219], v167 offset:50176
	ds_read_b64_tr_b16 v[220:221], v166 offset:57344
	ds_read_b64_tr_b16 v[222:223], v167 offset:58368
	s_add_u32 s74, s74, 0x10000
	s_waitcnt lgkmcnt(8)
	v_mfma_f32_16x16x32_bf16 v[182:185], v[192:195], v[62:65], 0
	s_addc_u32 s75, s75, 0
	s_mov_b64 s[76:77], 0x200
	v_lshl_add_u64 v[124:125], v[124:125], 0, s[4:5]
	v_mfma_f32_16x16x32_bf16 v[182:185], v[196:199], v[58:61], v[182:185]
	v_lshl_add_u64 v[126:127], v[126:127], 0, s[4:5]
	v_lshl_add_u64 v[128:129], v[128:129], 0, s[4:5]
	v_mfma_f32_16x16x32_bf16 v[182:185], v[200:203], v[54:57], v[182:185]
	global_load_dwordx2 v[190:191], v[190:191], off offset:-96
	v_lshl_add_u64 v[108:109], v[108:109], 0, s[4:5]
	v_mfma_f32_16x16x32_bf16 v[182:185], v[204:207], v[50:53], v[182:185]
	v_add_u32_e32 v180, 0x200, v180
	v_lshl_add_u64 v[116:117], v[116:117], 0, s[4:5]
	ds_read_b64_tr_b16 v[192:193], v168 offset:32768
	ds_read_b64_tr_b16 v[194:195], v169 offset:33792
	ds_read_b64_tr_b16 v[196:197], v168 offset:40960
	ds_read_b64_tr_b16 v[198:199], v169 offset:41984
	ds_read_b64_tr_b16 v[200:201], v168 offset:49152
	ds_read_b64_tr_b16 v[202:203], v169 offset:50176
	ds_read_b64_tr_b16 v[204:205], v168 offset:57344
	ds_read_b64_tr_b16 v[206:207], v169 offset:58368
	v_lshl_add_u64 v[118:119], v[118:119], 0, s[76:77]
	s_cmp_lg_u32 s74, 0x40000
	s_waitcnt vmcnt(7)
	v_lshlrev_b32_e32 v186, 16, v66
	v_and_b32_e32 v66, 0xffff0000, v66
	s_nop 0
	v_add_f32_e32 v183, v181, v183
	v_mul_f32_e32 v66, v183, v66
	v_mul_f32_e32 v183, 0x41800000, v66
	v_lshlrev_b32_e32 v66, 16, v67
	v_add_f32_e32 v184, v181, v184
	v_mul_f32_e32 v66, v184, v66
	v_add_f32_e32 v182, v181, v182
	v_mul_f32_e32 v184, 0x41800000, v66
	v_and_b32_e32 v66, 0xffff0000, v67
	v_add_f32_e32 v67, v181, v185
	v_mul_f32_e32 v182, v182, v186
	v_mul_f32_e32 v66, v67, v66
	v_mul_f32_e32 v182, 0x41800000, v182
	v_mul_f32_e32 v67, 0x41800000, v66
	v_cvt_pk_fp8_f32 v66, v182, v183
	v_cvt_pk_fp8_f32 v66, v184, v67 op_sel:[0,0,1]
	s_waitcnt lgkmcnt(8)
	v_mfma_f32_16x16x32_bf16 v[182:185], v[208:211], v[62:65], 0
	s_waitcnt vmcnt(0)
	v_lshlrev_b32_e32 v67, 16, v190
	v_mfma_f32_16x16x32_bf16 v[182:185], v[212:215], v[58:61], v[182:185]
	v_mfma_f32_16x16x32_bf16 v[182:185], v[216:219], v[54:57], v[182:185]
	v_mfma_f32_16x16x32_bf16 v[182:185], v[220:223], v[50:53], v[182:185]
	s_nop 7
	v_add_f32_e32 v182, v181, v182
	ds_read_b64_tr_b16 v[208:209], v170 offset:32768
	ds_read_b64_tr_b16 v[210:211], v171 offset:33792
	ds_read_b64_tr_b16 v[212:213], v170 offset:40960
	ds_read_b64_tr_b16 v[214:215], v171 offset:41984
	ds_read_b64_tr_b16 v[216:217], v170 offset:49152
	ds_read_b64_tr_b16 v[218:219], v171 offset:50176
	ds_read_b64_tr_b16 v[220:221], v170 offset:57344
	ds_read_b64_tr_b16 v[222:223], v171 offset:58368
	v_mul_f32_e32 v67, v182, v67
	v_mul_f32_e32 v182, 0x41800000, v67
	v_and_b32_e32 v67, 0xffff0000, v190
	v_add_f32_e32 v183, v181, v183
	v_mul_f32_e32 v67, v183, v67
	v_mul_f32_e32 v183, 0x41800000, v67
	v_lshlrev_b32_e32 v67, 16, v191
	v_add_f32_e32 v184, v181, v184
	v_mul_f32_e32 v67, v184, v67
	v_mul_f32_e32 v184, 0x41800000, v67
	v_and_b32_e32 v67, 0xffff0000, v191
	v_add_f32_e32 v185, v181, v185
	v_mul_f32_e32 v67, v185, v67
	v_mul_f32_e32 v185, 0x41800000, v67
	v_cvt_pk_fp8_f32 v67, v182, v183
	v_cvt_pk_fp8_f32 v67, v184, v185 op_sel:[0,0,1]
	s_waitcnt lgkmcnt(8)
	v_mfma_f32_16x16x32_bf16 v[182:185], v[192:195], v[62:65], 0
	v_permlane16_swap_b32_e32 v66, v67
	v_mfma_f32_16x16x32_bf16 v[182:185], v[196:199], v[58:61], v[182:185]
	v_mfma_f32_16x16x32_bf16 v[182:185], v[200:203], v[54:57], v[182:185]
	v_mfma_f32_16x16x32_bf16 v[182:185], v[204:207], v[50:53], v[182:185]
	v_lshlrev_b32_e32 v186, 16, v68
	v_and_b32_e32 v68, 0xffff0000, v68
	ds_read_b64_tr_b16 v[192:193], v172 offset:32768
	ds_read_b64_tr_b16 v[194:195], v173 offset:33792
	ds_read_b64_tr_b16 v[196:197], v172 offset:40960
	ds_read_b64_tr_b16 v[198:199], v173 offset:41984
	ds_read_b64_tr_b16 v[200:201], v172 offset:49152
	ds_read_b64_tr_b16 v[202:203], v173 offset:50176
	ds_read_b64_tr_b16 v[204:205], v172 offset:57344
	ds_read_b64_tr_b16 v[206:207], v173 offset:58368
	s_nop 5
	v_add_f32_e32 v183, v181, v183
	v_mul_f32_e32 v68, v183, v68
	v_mul_f32_e32 v183, 0x41800000, v68
	v_lshlrev_b32_e32 v68, 16, v69
	v_add_f32_e32 v184, v181, v184
	v_mul_f32_e32 v68, v184, v68
	v_add_f32_e32 v182, v181, v182
	v_mul_f32_e32 v184, 0x41800000, v68
	v_and_b32_e32 v68, 0xffff0000, v69
	v_add_f32_e32 v69, v181, v185
	v_mul_f32_e32 v182, v182, v186
	v_mul_f32_e32 v68, v69, v68
	v_mul_f32_e32 v182, 0x41800000, v182
	v_mul_f32_e32 v69, 0x41800000, v68
	v_cvt_pk_fp8_f32 v68, v182, v183
	v_cvt_pk_fp8_f32 v68, v184, v69 op_sel:[0,0,1]
	s_waitcnt lgkmcnt(8)
	v_mfma_f32_16x16x32_bf16 v[182:185], v[208:211], v[62:65], 0
	v_mfma_f32_16x16x32_bf16 v[182:185], v[212:215], v[58:61], v[182:185]
	v_mfma_f32_16x16x32_bf16 v[182:185], v[216:219], v[54:57], v[182:185]
	v_mfma_f32_16x16x32_bf16 v[182:185], v[220:223], v[50:53], v[182:185]
	s_nop 7
	v_add_f32_e32 v69, v181, v184
	ds_read_b64_tr_b16 v[208:209], v174 offset:32768
	ds_read_b64_tr_b16 v[210:211], v175 offset:33792
	ds_read_b64_tr_b16 v[212:213], v174 offset:40960
	ds_read_b64_tr_b16 v[214:215], v175 offset:41984
	ds_read_b64_tr_b16 v[216:217], v174 offset:49152
	ds_read_b64_tr_b16 v[218:219], v175 offset:50176
	ds_read_b64_tr_b16 v[220:221], v174 offset:57344
	ds_read_b64_tr_b16 v[222:223], v175 offset:58368
	v_lshlrev_b32_e32 v184, 16, v139
	v_mul_f32_e32 v69, v69, v184
	v_mul_f32_e32 v184, 0x41800000, v69
	v_add_f32_e32 v69, v181, v185
	v_and_b32_e32 v139, 0xffff0000, v139
	v_mul_f32_e32 v69, v69, v139
	v_mul_f32_e32 v139, 0x41800000, v69
	v_add_f32_e32 v69, v181, v182
	v_lshlrev_b32_e32 v182, 16, v138
	v_mul_f32_e32 v69, v69, v182
	v_mul_f32_e32 v182, 0x41800000, v69
	v_add_f32_e32 v69, v181, v183
	v_and_b32_e32 v138, 0xffff0000, v138
	v_mul_f32_e32 v69, v69, v138
	v_mul_f32_e32 v138, 0x41800000, v69
	v_cvt_pk_fp8_f32 v69, v182, v138
	v_cvt_pk_fp8_f32 v69, v184, v139 op_sel:[0,0,1]
	v_lshl_add_u64 v[138:139], s[92:93], 0, v[122:123]
	v_lshl_add_u64 v[122:123], v[122:123], 0, s[96:97]
	v_permlane16_swap_b32_e32 v68, v69
	s_nop 1
	v_permlane32_swap_b32_e32 v66, v68
	v_permlane32_swap_b32_e32 v67, v69
	global_store_dwordx4 v[138:139], v[66:69], off sc0 sc1
	s_nop 1
	s_waitcnt lgkmcnt(8)
	v_mfma_f32_16x16x32_bf16 v[66:69], v[192:195], v[62:65], 0
	v_lshlrev_b32_e32 v138, 16, v136
	v_mfma_f32_16x16x32_bf16 v[66:69], v[196:199], v[58:61], v[66:69]
	v_mfma_f32_16x16x32_bf16 v[66:69], v[200:203], v[54:57], v[66:69]
	v_mfma_f32_16x16x32_bf16 v[66:69], v[204:207], v[50:53], v[66:69]
	s_nop 7
	v_add_f32_e32 v66, v181, v66
	ds_read_b64_tr_b16 v[192:193], v176 offset:32768
	ds_read_b64_tr_b16 v[194:195], v177 offset:33792
	ds_read_b64_tr_b16 v[196:197], v176 offset:40960
	ds_read_b64_tr_b16 v[198:199], v177 offset:41984
	ds_read_b64_tr_b16 v[200:201], v176 offset:49152
	ds_read_b64_tr_b16 v[202:203], v177 offset:50176
	ds_read_b64_tr_b16 v[204:205], v176 offset:57344
	ds_read_b64_tr_b16 v[206:207], v177 offset:58368
	v_mul_f32_e32 v66, v66, v138
	v_mul_f32_e32 v138, 0x41800000, v66
	v_and_b32_e32 v66, 0xffff0000, v136
	v_add_f32_e32 v67, v181, v67
	v_mul_f32_e32 v66, v67, v66
	v_mul_f32_e32 v67, 0x41800000, v66
	v_lshlrev_b32_e32 v66, 16, v137
	v_add_f32_e32 v68, v181, v68
	v_mul_f32_e32 v66, v68, v66
	v_mul_f32_e32 v68, 0x41800000, v66
	v_and_b32_e32 v66, 0xffff0000, v137
	v_add_f32_e32 v69, v181, v69
	v_mul_f32_e32 v66, v69, v66
	v_mul_f32_e32 v69, 0x41800000, v66
	v_cvt_pk_fp8_f32 v66, v138, v67
	s_waitcnt lgkmcnt(8)
	v_mfma_f32_16x16x32_bf16 v[136:139], v[208:211], v[62:65], 0
	v_cvt_pk_fp8_f32 v66, v68, v69 op_sel:[0,0,1]
	v_lshlrev_b32_e32 v67, 16, v134
	v_mfma_f32_16x16x32_bf16 v[136:139], v[212:215], v[58:61], v[136:139]
	v_mfma_f32_16x16x32_bf16 v[136:139], v[216:219], v[54:57], v[136:139]
	v_mfma_f32_16x16x32_bf16 v[136:139], v[220:223], v[50:53], v[136:139]
	s_nop 7
	v_add_f32_e32 v68, v181, v136
	ds_read_b64_tr_b16 v[208:209], v178 offset:32768
	ds_read_b64_tr_b16 v[210:211], v179 offset:33792
	ds_read_b64_tr_b16 v[212:213], v178 offset:40960
	ds_read_b64_tr_b16 v[214:215], v179 offset:41984
	ds_read_b64_tr_b16 v[216:217], v178 offset:49152
	ds_read_b64_tr_b16 v[218:219], v179 offset:50176
	ds_read_b64_tr_b16 v[220:221], v178 offset:57344
	ds_read_b64_tr_b16 v[222:223], v179 offset:58368
	v_mul_f32_e32 v67, v68, v67
	v_mul_f32_e32 v68, 0x41800000, v67
	v_and_b32_e32 v67, 0xffff0000, v134
	v_add_f32_e32 v69, v181, v137
	v_mul_f32_e32 v67, v69, v67
	v_mul_f32_e32 v69, 0x41800000, v67
	v_lshlrev_b32_e32 v67, 16, v135
	v_add_f32_e32 v134, v181, v138
	v_mul_f32_e32 v67, v134, v67
	v_mul_f32_e32 v134, 0x41800000, v67
	v_and_b32_e32 v67, 0xffff0000, v135
	v_add_f32_e32 v135, v181, v139
	v_mul_f32_e32 v67, v135, v67
	v_mul_f32_e32 v135, 0x41800000, v67
	v_cvt_pk_fp8_f32 v67, v68, v69
	v_lshlrev_b32_e32 v68, 16, v132
	v_cvt_pk_fp8_f32 v67, v134, v135 op_sel:[0,0,1]
	s_waitcnt lgkmcnt(8)
	v_mfma_f32_16x16x32_bf16 v[134:137], v[192:195], v[62:65], 0
	v_permlane16_swap_b32_e32 v66, v67
	v_mfma_f32_16x16x32_bf16 v[134:137], v[196:199], v[58:61], v[134:137]
	v_mfma_f32_16x16x32_bf16 v[134:137], v[200:203], v[54:57], v[134:137]
	v_mfma_f32_16x16x32_bf16 v[134:137], v[204:207], v[50:53], v[134:137]
	s_nop 7
	v_add_f32_e32 v69, v181, v134
	v_mul_f32_e32 v68, v69, v68
	v_mul_f32_e32 v69, 0x41800000, v68
	v_and_b32_e32 v68, 0xffff0000, v132
	v_add_f32_e32 v132, v181, v135
	v_mul_f32_e32 v68, v132, v68
	v_mul_f32_e32 v132, 0x41800000, v68
	v_lshlrev_b32_e32 v68, 16, v133
	v_add_f32_e32 v134, v181, v136
	v_mul_f32_e32 v68, v134, v68
	v_mul_f32_e32 v134, 0x41800000, v68
	v_and_b32_e32 v68, 0xffff0000, v133
	v_add_f32_e32 v133, v181, v137
	v_mul_f32_e32 v68, v133, v68
	v_mul_f32_e32 v133, 0x41800000, v68
	v_cvt_pk_fp8_f32 v68, v69, v132
	v_cvt_pk_fp8_f32 v68, v134, v133 op_sel:[0,0,1]
	s_waitcnt lgkmcnt(0)
	v_mfma_f32_16x16x32_bf16 v[62:65], v[208:211], v[62:65], 0
	v_mfma_f32_16x16x32_bf16 v[58:61], v[212:215], v[58:61], v[62:65]
	s_nop 3
	v_mfma_f32_16x16x32_bf16 v[54:57], v[216:219], v[54:57], v[58:61]
	s_nop 2
	v_mfma_f32_16x16x32_bf16 v[50:53], v[220:223], v[50:53], v[54:57]
	s_nop 2
	v_lshlrev_b32_e32 v54, 16, v131
	s_nop 3
	v_add_f32_e32 v52, v181, v52
	v_mul_f32_e32 v52, v52, v54
	v_add_f32_e32 v53, v181, v53
	v_and_b32_e32 v54, 0xffff0000, v131
	v_mul_f32_e32 v53, v53, v54
	v_add_f32_e32 v50, v181, v50
	v_lshlrev_b32_e32 v54, 16, v130
	v_mul_f32_e32 v50, v50, v54
	v_add_f32_e32 v51, v181, v51
	v_and_b32_e32 v54, 0xffff0000, v130
	v_mul_f32_e32 v51, v51, v54
	v_mul_f32_e32 v50, 0x41800000, v50
	v_mul_f32_e32 v51, 0x41800000, v51
	v_cvt_pk_fp8_f32 v69, v50, v51
	v_mul_f32_e32 v52, 0x41800000, v52
	v_mul_f32_e32 v53, 0x41800000, v53
	v_lshl_add_u64 v[50:51], s[92:93], 0, v[120:121]
	v_cvt_pk_fp8_f32 v69, v52, v53 op_sel:[0,0,1]
	v_lshl_add_u64 v[120:121], v[120:121], 0, s[96:97]
	s_nop 0
	v_permlane16_swap_b32_e32 v68, v69
	s_nop 1
	v_permlane32_swap_b32_e32 v66, v68
	v_permlane32_swap_b32_e32 v67, v69
	global_store_dwordx4 v[50:51], v[66:69], off sc0 sc1
	s_barrier
	s_cbranch_scc0 .LBB0_330

.LBB0_396:
	v_add_u32_e32 v10, s86, v157
	v_add_u32_e32 v252, v10, v149
	ds_read_b64_tr_b16 v[188:189], v252 offset:32768
	ds_read_b64_tr_b16 v[190:191], v252 offset:36864
	v_add_u32_e32 v253, v10, v151
	ds_read_b64_tr_b16 v[192:193], v253 offset:32768
	ds_read_b64_tr_b16 v[194:195], v253 offset:36864
	v_add_u32_e32 v252, v10, v150
	ds_read_b64_tr_b16 v[196:197], v252 offset:32768
	ds_read_b64_tr_b16 v[198:199], v252 offset:36864
	v_add_u32_e32 v253, v10, v153
	ds_read_b64_tr_b16 v[200:201], v253 offset:32768
	ds_read_b64_tr_b16 v[202:203], v253 offset:36864
	v_add_u32_e32 v252, v10, v152
	ds_read_b64_tr_b16 v[204:205], v252 offset:32768
	ds_read_b64_tr_b16 v[206:207], v252 offset:36864
	v_add_u32_e32 v253, v10, v155
	ds_read_b64_tr_b16 v[208:209], v253 offset:32768
	ds_read_b64_tr_b16 v[210:211], v253 offset:36864
	v_add_u32_e32 v252, v10, v154
	ds_read_b64_tr_b16 v[212:213], v252 offset:32768
	ds_read_b64_tr_b16 v[214:215], v252 offset:36864
	v_add_u32_e32 v253, v10, v156
	ds_read_b64_tr_b16 v[216:217], v253 offset:32768
	ds_read_b64_tr_b16 v[218:219], v253 offset:36864
	v_cvt_pk_bf16_f32 v82, v81, v82
	v_cvt_pk_bf16_f32 v83, v83, v84
	v_cvt_pk_bf16_f32 v84, v85, v86
	v_cvt_pk_bf16_f32 v85, v87, v89
	s_nop 1
	s_waitcnt lgkmcnt(14)
	v_mfma_f32_16x16x32_bf16 v[86:89], v[188:191], v[82:85], v[2:5]
	s_waitcnt lgkmcnt(12)
	v_mfma_f32_16x16x32_bf16 v[58:61], v[192:195], v[82:85], v[58:61]
	s_ashr_i32 s43, s42, 31
	s_waitcnt lgkmcnt(10)
	v_mfma_f32_16x16x32_bf16 v[6:9], v[196:199], v[82:85], v[6:9]
	s_waitcnt lgkmcnt(8)
	v_mfma_f32_16x16x32_bf16 v[66:69], v[200:203], v[82:85], v[66:69]
	s_lshl_b64 s[16:17], s[42:43], 11
	s_waitcnt lgkmcnt(6)
	v_mfma_f32_16x16x32_bf16 v[62:65], v[204:207], v[82:85], v[62:65]
	s_waitcnt lgkmcnt(4)
	v_mfma_f32_16x16x32_bf16 v[70:73], v[208:211], v[82:85], v[70:73]
	v_add_f32_e32 v4, v79, v80
	v_rcp_f32_e32 v5, v4
	s_waitcnt lgkmcnt(2)
	v_mfma_f32_16x16x32_bf16 v[74:77], v[212:215], v[82:85], v[74:77]
	v_lshl_add_u32 v10, s5, 7, v108
	v_mul_lo_u32 v2, v10, s30
	v_mul_f32_e32 v10, v5, v86
	v_mul_f32_e32 v79, v5, v87
	v_mul_f32_e32 v6, v5, v6
	v_mul_f32_e32 v7, v5, v7
	v_cvt_pk_fp8_f32 v80, v10, v79
	v_cvt_pk_fp8_f32 v81, v6, v7
	s_waitcnt lgkmcnt(0)
	v_mfma_f32_16x16x32_bf16 v[54:57], v[216:219], v[82:85], v[54:57]
	v_mul_f32_e32 v82, v5, v88
	v_mul_f32_e32 v83, v5, v89
	v_mul_f32_e32 v6, v5, v8
	v_mul_f32_e32 v7, v5, v9
	v_cvt_pk_fp8_f32 v80, v82, v83 op_sel:[0,0,1]
	v_cvt_pk_fp8_f32 v81, v6, v7 op_sel:[0,0,1]
	v_mul_f32_e32 v6, v5, v58
	v_mul_f32_e32 v7, v5, v59
	v_cvt_pk_fp8_f32 v82, v6, v7
	v_mul_f32_e32 v6, v5, v62
	v_mul_f32_e32 v7, v5, v63
	v_cvt_pk_fp8_f32 v83, v6, v7
	v_mul_f32_e32 v8, v5, v60
	v_mul_f32_e32 v9, v5, v61
	v_mul_f32_e32 v6, v5, v64
	v_mul_f32_e32 v7, v5, v65
	v_cvt_pk_fp8_f32 v82, v8, v9 op_sel:[0,0,1]
	v_cvt_pk_fp8_f32 v83, v6, v7 op_sel:[0,0,1]
	v_mul_f32_e32 v7, v5, v66
	v_mul_f32_e32 v8, v5, v67
	v_cvt_pk_fp8_f32 v6, v7, v8
	v_mul_f32_e32 v8, v5, v74
	v_mul_f32_e32 v58, v5, v75
	v_cvt_pk_fp8_f32 v7, v8, v58
	v_mul_f32_e32 v9, v5, v68
	v_mul_f32_e32 v10, v5, v69
	v_cvt_pk_fp8_f32 v6, v9, v10 op_sel:[0,0,1]
	v_mul_f32_e32 v8, v5, v76
	v_mul_f32_e32 v9, v5, v77
	v_cvt_pk_fp8_f32 v7, v8, v9 op_sel:[0,0,1]
	v_mul_f32_e32 v9, v5, v70
	v_mul_f32_e32 v10, v5, v71
	v_cvt_pk_fp8_f32 v8, v9, v10
	v_mul_f32_e32 v10, v5, v54
	v_mul_f32_e32 v54, v5, v55
	v_cvt_pk_fp8_f32 v9, v10, v54
	s_ashr_i32 s5, s4, 31
	s_lshl_b64 s[4:5], s[4:5], 14
	v_add_u32_e32 v2, s1, v2
	s_add_u32 s4, s4, s16
	v_mul_f32_e32 v58, v5, v72
	v_mul_f32_e32 v59, v5, v73
	v_mul_f32_e32 v10, v5, v56
	v_mul_f32_e32 v5, v5, v57
	v_ashrrev_i32_e32 v3, 31, v2
	s_addc_u32 s5, s5, s17
	v_cvt_pk_fp8_f32 v8, v58, v59 op_sel:[0,0,1]
	v_cvt_pk_fp8_f32 v9, v10, v5 op_sel:[0,0,1]
	v_lshl_add_u64 v[2:3], s[4:5], 0, v[2:3]
	v_lshlrev_b64 v[12:13], 10, v[2:3]
	s_lshl_b32 s30, s0, 7
	v_lshl_add_u64 v[12:13], s[34:35], 0, v[12:13]
	v_lshl_add_u64 v[12:13], v[12:13], 0, s[30:31]
	v_permlane16_swap_b32_e32 v80, v81
	v_permlane16_swap_b32_e32 v82, v83
	v_permlane16_swap_b32_e32 v6, v7
	v_permlane16_swap_b32_e32 v8, v9
	v_permlane32_swap_b32_e32 v80, v82
	v_permlane32_swap_b32_e32 v81, v83
	v_lshl_add_u64 v[12:13], v[12:13], 0, v[100:101]
	v_permlane32_swap_b32_e32 v6, v8
	v_permlane32_swap_b32_e32 v7, v9
	global_store_dwordx4 v[12:13], v[80:83], off sc0 sc1
	global_store_dwordx4 v[12:13], v[6:9], off offset:64 sc0 sc1
	s_and_saveexec_b64 s[4:5], s[8:9]
	s_cbranch_execz .LBB0_354
	v_log_f32_e32 v4, v4
	v_lshlrev_b64 v[2:3], 5, v[2:3]
	s_mov_b32 s1, s31
	v_lshl_add_u64 v[2:3], s[40:41], 0, v[2:3]
	v_add_f32_e32 v4, v78, v4
	v_mul_f32_e32 v4, 0x3f317218, v4
	v_lshl_add_u64 v[2:3], s[0:1], 2, v[2:3]
	global_store_dword v[2:3], v4, off
	s_branch .LBB0_354

.LBB0_457:
	v_alignbit_b32 v24, v3, v2, 1
	v_add_co_u32_e32 v16, vcc, s3, v6
	v_and_b32_e32 v4, 0x7ffe0, v24
	s_nop 0
	v_addc_co_u32_e32 v17, vcc, 0, v7, vcc
	v_add_co_u32_e32 v20, vcc, s14, v6
	v_lshl_add_u64 v[22:23], s[4:5], 0, v[4:5]
	v_and_b32_e32 v4, 28, v24
	v_addc_co_u32_e32 v21, vcc, 0, v7, vcc
	v_lshl_add_u64 v[22:23], v[22:23], 0, v[4:5]
	v_add_co_u32_e32 v24, vcc, 0x80000, v22
	global_load_dword v4, v[22:23], off
	s_nop 0
	v_addc_co_u32_e32 v25, vcc, 0, v23, vcc
	v_add_co_u32_e32 v22, vcc, 0x100000, v22
	global_load_dwordx4 v[8:11], v[6:7], off
	s_nop 0
	v_addc_co_u32_e32 v23, vcc, 0, v23, vcc
	global_load_dwordx4 v[16:19], v[16:17], off
	s_nop 0
	global_load_dword v60, v[24:25], off
	global_load_dword v61, v[22:23], off
	s_nop 0
	global_load_dwordx4 v[20:23], v[20:21], off
	v_lshl_add_u64 v[2:3], v[2:3], 0, s[6:7]
	v_cmp_lt_u64_e32 vcc, s[12:13], v[2:3]
	s_or_b64 s[10:11], vcc, s[10:11]
	s_waitcnt vmcnt(0)
	v_cvt_pk_f32_fp8_e32 v[24:25], v8
	v_cvt_pk_f32_fp8_sdwa v[26:27], v8 src0_sel:WORD_1
	v_cvt_pk_f32_fp8_e32 v[28:29], v9
	v_max3_f32 v62, v4, v60, v61
	v_sub_f32_e32 v4, v4, v62
	v_sub_f32_e32 v60, v60, v62
	v_sub_f32_e32 v61, v61, v62
	v_mul_f32_e32 v4, 0x3fb8aa3b, v4
	v_mul_f32_e32 v60, 0x3fb8aa3b, v60
	v_mul_f32_e32 v61, 0x3fb8aa3b, v61
	v_exp_f32_e32 v4, v4
	v_exp_f32_e32 v62, v60
	v_exp_f32_e32 v61, v61
	v_cvt_pk_f32_fp8_e32 v[36:37], v16
	v_cvt_pk_f32_fp8_sdwa v[40:41], v16 src0_sel:WORD_1
	v_add_f32_e32 v60, v4, v62
	v_add_f32_e32 v63, v61, v60
	v_div_scale_f32 v60, s[16:17], v63, v63, 1.0
	v_rcp_f32_e32 v65, v60
	v_div_scale_f32 v64, vcc, 1.0, v63, 1.0
	v_cvt_pk_f32_fp8_e32 v[44:45], v17
	v_fma_f32 v66, -v60, v65, 1.0
	v_fmac_f32_e32 v65, v66, v65
	v_mul_f32_e32 v66, v64, v65
	v_fma_f32 v67, -v60, v66, v64
	v_fmac_f32_e32 v66, v67, v65
	v_cvt_pk_f32_fp8_sdwa v[16:17], v17 src0_sel:WORD_1
	v_cvt_pk_f32_fp8_e32 v[48:49], v18
	v_cvt_pk_f32_fp8_sdwa v[52:53], v18 src0_sel:WORD_1
	v_cvt_pk_f32_fp8_e32 v[56:57], v19
	v_fma_f32 v60, -v60, v66, v64
	v_cvt_pk_f32_fp8_sdwa v[8:9], v9 src0_sel:WORD_1
	v_cvt_pk_f32_fp8_e32 v[30:31], v10
	v_cvt_pk_f32_fp8_sdwa v[32:33], v10 src0_sel:WORD_1
	v_cvt_pk_f32_fp8_e32 v[34:35], v11
	v_cvt_pk_f32_fp8_sdwa v[18:19], v19 src0_sel:WORD_1
	v_div_fmas_f32 v64, v60, v65, v66
	v_cvt_pk_f32_fp8_sdwa v[10:11], v11 src0_sel:WORD_1
	v_cvt_pk_f32_fp8_e32 v[38:39], v20
	v_cvt_pk_f32_fp8_sdwa v[42:43], v20 src0_sel:WORD_1
	v_cvt_pk_f32_fp8_e32 v[46:47], v21
	v_cvt_pk_f32_fp8_e32 v[50:51], v22
	v_cvt_pk_f32_fp8_e32 v[58:59], v23
	v_div_fixup_f32 v63, v64, v63, 1.0
	v_mul_f32_e32 v62, v62, v63
	v_mul_f32_e32 v4, v4, v63
	v_pk_mul_f32 v[36:37], v[62:63], v[36:37] op_sel_hi:[0,1]
	v_pk_mul_f32 v[40:41], v[62:63], v[40:41] op_sel_hi:[0,1]
	v_pk_mul_f32 v[44:45], v[62:63], v[44:45] op_sel_hi:[0,1]
	v_pk_mul_f32 v[16:17], v[62:63], v[16:17] op_sel_hi:[0,1]
	v_pk_mul_f32 v[48:49], v[62:63], v[48:49] op_sel_hi:[0,1]
	v_pk_mul_f32 v[52:53], v[62:63], v[52:53] op_sel_hi:[0,1]
	v_pk_mul_f32 v[56:57], v[62:63], v[56:57] op_sel_hi:[0,1]
	v_mul_f32_e32 v64, v61, v63
	v_pk_mul_f32 v[18:19], v[62:63], v[18:19] op_sel_hi:[0,1]
	v_pk_fma_f32 v[24:25], v[4:5], v[24:25], v[36:37] op_sel_hi:[0,1,1]
	v_pk_fma_f32 v[26:27], v[4:5], v[26:27], v[40:41] op_sel_hi:[0,1,1]
	v_pk_fma_f32 v[28:29], v[4:5], v[28:29], v[44:45] op_sel_hi:[0,1,1]
	v_pk_fma_f32 v[8:9], v[4:5], v[8:9], v[16:17] op_sel_hi:[0,1,1]
	v_pk_fma_f32 v[16:17], v[4:5], v[30:31], v[48:49] op_sel_hi:[0,1,1]
	v_pk_fma_f32 v[30:31], v[4:5], v[32:33], v[52:53] op_sel_hi:[0,1,1]
	v_pk_fma_f32 v[32:33], v[4:5], v[34:35], v[56:57] op_sel_hi:[0,1,1]
	v_cvt_pk_f32_fp8_sdwa v[20:21], v21 src0_sel:WORD_1
	v_cvt_pk_f32_fp8_sdwa v[54:55], v22 src0_sel:WORD_1
	v_cvt_pk_f32_fp8_sdwa v[22:23], v23 src0_sel:WORD_1
	v_pk_fma_f32 v[10:11], v[4:5], v[10:11], v[18:19] op_sel_hi:[0,1,1]
	v_pk_fma_f32 v[18:19], v[64:65], v[38:39], v[24:25] op_sel_hi:[0,1,1]
	v_pk_fma_f32 v[24:25], v[64:65], v[42:43], v[26:27] op_sel_hi:[0,1,1]
	v_pk_fma_f32 v[26:27], v[64:65], v[46:47], v[28:29] op_sel_hi:[0,1,1]
	v_pk_fma_f32 v[16:17], v[64:65], v[50:51], v[16:17] op_sel_hi:[0,1,1]
	v_pk_fma_f32 v[28:29], v[64:65], v[58:59], v[32:33] op_sel_hi:[0,1,1]
	v_cvt_pk_fp8_f32 v12, v18, v19
	v_cvt_pk_fp8_f32 v13, v26, v27
	v_cvt_pk_fp8_f32 v14, v16, v17
	v_cvt_pk_fp8_f32 v15, v28, v29
	v_pk_fma_f32 v[8:9], v[64:65], v[20:21], v[8:9] op_sel_hi:[0,1,1]
	v_pk_fma_f32 v[20:21], v[64:65], v[54:55], v[30:31] op_sel_hi:[0,1,1]
	v_pk_fma_f32 v[10:11], v[64:65], v[22:23], v[10:11] op_sel_hi:[0,1,1]
	v_cvt_pk_fp8_f32 v12, v24, v25 op_sel:[0,0,1]
	v_cvt_pk_fp8_f32 v13, v8, v9 op_sel:[0,0,1]
	v_cvt_pk_fp8_f32 v14, v20, v21 op_sel:[0,0,1]
	v_cvt_pk_fp8_f32 v15, v10, v11 op_sel:[0,0,1]
	v_add_co_u32_e32 v60, vcc, 0x6000000, v6
	s_nop 1
	v_addc_co_u32_e32 v61, vcc, 0, v7, vcc
	v_lshl_add_u64 v[6:7], v[6:7], 0, s[8:9]
	global_store_dwordx4 v[60:61], v[12:15], off sc0 sc1
	s_andn2_b64 exec, exec, s[10:11]
	s_cbranch_execnz .LBB0_457

.LBB0_706:
	v_lshl_add_u64 v[8:9], s[92:93], 0, v[4:5]
	v_add_co_u32_e32 v10, vcc, 0x69400000, v8
	v_mov_b32_e32 v144, 0
	s_nop 0
	v_addc_co_u32_e32 v11, vcc, 0, v9, vcc
	v_add_co_u32_e32 v8, vcc, s43, v8
	v_lshl_add_u32 v144, v144, 2, v132
	s_nop 0
	v_addc_co_u32_e32 v9, vcc, 0, v9, vcc
	s_waitcnt vmcnt(16)
	v_lshlrev_b32_e32 v6, 16, v160
	v_and_b32_e32 v7, 0xffff0000, v160
	v_lshlrev_b32_e32 v70, 16, v161
	v_and_b32_e32 v71, 0xffff0000, v161
	v_add_f32_e32 v12, v6, v7
	v_add_f32_e32 v13, v70, v71
	v_add_f32_e32 v12, v12, v13
	v_add_f32_e32 v14, 0, v12
	v_lshlrev_b32_e32 v66, 16, v162
	v_and_b32_e32 v67, 0xffff0000, v162
	v_lshlrev_b32_e32 v68, 16, v163
	v_and_b32_e32 v69, 0xffff0000, v163
	v_add_f32_e32 v12, v66, v67
	v_add_f32_e32 v13, v68, v69
	v_add_f32_e32 v12, v12, v13
	v_add_f32_e32 v14, v14, v12
	v_lshlrev_b32_e32 v64, 16, v164
	v_and_b32_e32 v65, 0xffff0000, v164
	v_lshlrev_b32_e32 v62, 16, v165
	v_and_b32_e32 v63, 0xffff0000, v165
	v_add_f32_e32 v12, v64, v65
	v_add_f32_e32 v13, v62, v63
	v_add_f32_e32 v12, v12, v13
	v_add_f32_e32 v14, v14, v12
	v_lshlrev_b32_e32 v58, 16, v166
	v_and_b32_e32 v59, 0xffff0000, v166
	v_lshlrev_b32_e32 v60, 16, v167
	v_and_b32_e32 v61, 0xffff0000, v167
	v_add_f32_e32 v12, v58, v59
	v_add_f32_e32 v13, v60, v61
	v_add_f32_e32 v12, v12, v13
	v_add_f32_e32 v14, v14, v12
	v_lshlrev_b32_e32 v56, 16, v168
	v_and_b32_e32 v57, 0xffff0000, v168
	v_lshlrev_b32_e32 v54, 16, v169
	v_and_b32_e32 v55, 0xffff0000, v169
	v_add_f32_e32 v12, v56, v57
	v_add_f32_e32 v13, v54, v55
	v_add_f32_e32 v12, v12, v13
	v_add_f32_e32 v14, v14, v12
	v_lshlrev_b32_e32 v32, 16, v170
	v_and_b32_e32 v33, 0xffff0000, v170
	v_lshlrev_b32_e32 v52, 16, v171
	v_and_b32_e32 v53, 0xffff0000, v171
	v_add_f32_e32 v12, v32, v33
	v_add_f32_e32 v13, v52, v53
	v_add_f32_e32 v12, v12, v13
	v_add_f32_e32 v14, v14, v12
	v_lshlrev_b32_e32 v30, 16, v172
	v_and_b32_e32 v31, 0xffff0000, v172
	v_lshlrev_b32_e32 v28, 16, v173
	v_and_b32_e32 v29, 0xffff0000, v173
	v_add_f32_e32 v12, v30, v31
	v_add_f32_e32 v13, v28, v29
	v_add_f32_e32 v12, v12, v13
	v_add_f32_e32 v12, v14, v12
	v_lshlrev_b32_e32 v24, 16, v174
	v_and_b32_e32 v25, 0xffff0000, v174
	v_lshlrev_b32_e32 v26, 16, v175
	v_and_b32_e32 v27, 0xffff0000, v175
	v_add_f32_e32 v10, v24, v25
	v_add_f32_e32 v11, v26, v27
	v_add_f32_e32 v10, v10, v11
	v_add_f32_e32 v34, v12, v10
	global_load_dwordx2 v[22:23], v[8:9], off
	global_load_dwordx2 v[20:21], v[8:9], off offset:512
	global_load_dwordx2 v[18:19], v[8:9], off offset:1024
	global_load_dwordx2 v[16:17], v[8:9], off offset:1536
	global_load_dwordx2 v[14:15], v[8:9], off offset:2048
	global_load_dwordx2 v[12:13], v[8:9], off offset:2560
	global_load_dwordx2 v[10:11], v[8:9], off offset:3072
	s_nop 0
	global_load_dwordx2 v[8:9], v[8:9], off offset:3584
	s_cmp_lt_i32 s36, 4
	s_cselect_b32 s12, s30, 0
	s_cselect_b32 s13, s31, 0
	v_lshl_add_u64 v[176:177], v[4:5], 0, s[12:13]
	v_lshl_add_u64 v[176:177], s[92:93], 0, v[176:177]
	s_mov_b32 s12, 0x69400000
	s_mov_b32 s13, 0
	v_lshl_add_u64 v[176:177], v[176:177], 0, s[12:13]
	global_load_dwordx2 v[160:161], v[176:177], off
	global_load_dwordx2 v[162:163], v[176:177], off offset:512
	global_load_dwordx2 v[164:165], v[176:177], off offset:1024
	global_load_dwordx2 v[166:167], v[176:177], off offset:1536
	global_load_dwordx2 v[168:169], v[176:177], off offset:2048
	global_load_dwordx2 v[170:171], v[176:177], off offset:2560
	global_load_dwordx2 v[172:173], v[176:177], off offset:3072
	global_load_dwordx2 v[174:175], v[176:177], off offset:3584
	v_add_f32_dpp v34, v34, v34 quad_perm:[1,0,3,2] row_mask:0xf bank_mask:0xf bound_ctrl:1
	s_nop 1
	v_add_f32_dpp v34, v34, v34 quad_perm:[2,3,0,1] row_mask:0xf bank_mask:0xf bound_ctrl:1
	s_nop 1
	v_add_f32_dpp v34, v34, v34 row_half_mirror row_mask:0xf bank_mask:0xf bound_ctrl:1
	s_nop 1
	v_add_f32_dpp v34, v34, v34 row_mirror row_mask:0xf bank_mask:0xf bound_ctrl:1
	v_mov_b32_e32 v145, v34
	s_nop 1
	v_permlane16_swap_b32_e32 v34, v145
	v_add_f32_e32 v34, v34, v145
	v_mov_b32_e32 v145, v34
	s_nop 1
	v_permlane32_swap_b32_e32 v34, v145
	v_add_f32_e32 v145, v34, v145
	v_fmac_f32_e32 v71, 0xba000000, v145
	v_fmac_f32_e32 v7, 0xba000000, v145
	v_fmac_f32_e32 v70, 0xba000000, v145
	v_fmac_f32_e32 v6, 0xba000000, v145
	v_mul_f32_e32 v34, v7, v7
	v_mul_f32_e32 v146, v71, v71
	v_fmac_f32_e32 v34, v6, v6
	v_fmac_f32_e32 v146, v70, v70
	v_fmac_f32_e32 v69, 0xba000000, v145
	v_fmac_f32_e32 v67, 0xba000000, v145
	v_add_f32_e32 v34, v34, v146
	v_fmac_f32_e32 v68, 0xba000000, v145
	v_fmac_f32_e32 v66, 0xba000000, v145
	v_mul_f32_e32 v146, v67, v67
	v_mul_f32_e32 v147, v69, v69
	v_fmac_f32_e32 v146, v66, v66
	v_fmac_f32_e32 v147, v68, v68
	v_add_f32_e32 v146, v146, v147
	v_fmac_f32_e32 v63, 0xba000000, v145
	v_fmac_f32_e32 v65, 0xba000000, v145
	v_add_f32_e32 v34, v34, v146
	v_fmac_f32_e32 v62, 0xba000000, v145
	v_fmac_f32_e32 v64, 0xba000000, v145
	v_mul_f32_e32 v146, v65, v65
	v_mul_f32_e32 v147, v63, v63
	v_fmac_f32_e32 v146, v64, v64
	v_fmac_f32_e32 v147, v62, v62
	v_add_f32_e32 v146, v146, v147
	v_fmac_f32_e32 v61, 0xba000000, v145
	v_fmac_f32_e32 v59, 0xba000000, v145
	v_add_f32_e32 v34, v146, v34
	v_fmac_f32_e32 v60, 0xba000000, v145
	v_fmac_f32_e32 v58, 0xba000000, v145
	v_mul_f32_e32 v146, v59, v59
	v_mul_f32_e32 v147, v61, v61
	v_fmac_f32_e32 v146, v58, v58
	v_fmac_f32_e32 v147, v60, v60
	v_add_f32_e32 v146, v146, v147
	v_fmac_f32_e32 v55, 0xba000000, v145
	v_fmac_f32_e32 v57, 0xba000000, v145
	v_add_f32_e32 v34, v146, v34
	v_fmac_f32_e32 v54, 0xba000000, v145
	v_fmac_f32_e32 v56, 0xba000000, v145
	v_mul_f32_e32 v146, v57, v57
	v_mul_f32_e32 v147, v55, v55
	v_fmac_f32_e32 v146, v56, v56
	v_fmac_f32_e32 v147, v54, v54
	v_add_f32_e32 v146, v146, v147
	v_fmac_f32_e32 v53, 0xba000000, v145
	v_fmac_f32_e32 v33, 0xba000000, v145
	v_add_f32_e32 v34, v146, v34
	v_fmac_f32_e32 v52, 0xba000000, v145
	v_fmac_f32_e32 v32, 0xba000000, v145
	v_mul_f32_e32 v146, v33, v33
	v_mul_f32_e32 v147, v53, v53
	v_fmac_f32_e32 v146, v32, v32
	v_fmac_f32_e32 v147, v52, v52
	v_add_f32_e32 v146, v146, v147
	v_fmac_f32_e32 v29, 0xba000000, v145
	v_fmac_f32_e32 v31, 0xba000000, v145
	v_add_f32_e32 v34, v146, v34
	v_fmac_f32_e32 v28, 0xba000000, v145
	v_fmac_f32_e32 v30, 0xba000000, v145
	v_mul_f32_e32 v146, v31, v31
	v_mul_f32_e32 v147, v29, v29
	v_fmac_f32_e32 v146, v30, v30
	v_fmac_f32_e32 v147, v28, v28
	v_add_f32_e32 v146, v146, v147
	v_fmac_f32_e32 v27, 0xba000000, v145
	v_fmac_f32_e32 v25, 0xba000000, v145
	v_add_f32_e32 v34, v146, v34
	v_fmac_f32_e32 v26, 0xba000000, v145
	v_fmac_f32_e32 v24, 0xba000000, v145
	v_mul_f32_e32 v146, v25, v25
	v_mul_f32_e32 v147, v27, v27
	v_fmac_f32_e32 v146, v24, v24
	v_fmac_f32_e32 v147, v26, v26
	v_add_f32_e32 v146, v146, v147
	v_add_f32_e32 v34, v146, v34
	s_nop 1
	v_add_f32_dpp v34, v34, v34 quad_perm:[1,0,3,2] row_mask:0xf bank_mask:0xf bound_ctrl:1
	s_nop 1
	v_add_f32_dpp v34, v34, v34 quad_perm:[2,3,0,1] row_mask:0xf bank_mask:0xf bound_ctrl:1
	s_nop 1
	v_add_f32_dpp v34, v34, v34 row_half_mirror row_mask:0xf bank_mask:0xf bound_ctrl:1
	s_nop 1
	v_add_f32_dpp v34, v34, v34 row_mirror row_mask:0xf bank_mask:0xf bound_ctrl:1
	v_mov_b32_e32 v146, v34
	s_nop 1
	v_permlane16_swap_b32_e32 v34, v146
	v_add_f32_e32 v34, v34, v146
	v_mov_b32_e32 v146, v34
	s_nop 1
	v_permlane32_swap_b32_e32 v34, v146
	v_add_f32_e32 v34, v34, v146
	v_fmamk_f32 v34, v34, 0x3a000000, v135
	v_cmp_gt_f32_e32 vcc, s44, v34
	v_mul_f32_e32 v146, 0x4f800000, v34
	s_nop 0
	v_cndmask_b32_e32 v34, v34, v146, vcc
	v_sqrt_f32_e32 v146, v34
	s_nop 0
	v_add_u32_e32 v147, -1, v146
	v_fma_f32 v148, -v147, v146, v34
	v_cmp_ge_f32_e64 s[12:13], 0, v148
	v_add_u32_e32 v148, 1, v146
	s_nop 0
	v_cndmask_b32_e64 v147, v146, v147, s[12:13]
	v_fma_f32 v146, -v148, v146, v34
	v_cmp_lt_f32_e64 s[12:13], 0, v146
	s_nop 1
	v_cndmask_b32_e64 v146, v147, v148, s[12:13]
	v_mul_f32_e32 v147, 0x37800000, v146
	v_cndmask_b32_e32 v146, v146, v147, vcc
	v_cmp_class_f32_e32 vcc, v34, v136
	s_nop 1
	v_cndmask_b32_e32 v34, v146, v34, vcc
	v_div_scale_f32 v146, s[12:13], v34, v34, 1.0
	v_rcp_f32_e32 v147, v146
	s_nop 0
	v_fma_f32 v148, -v146, v147, 1.0
	v_fmac_f32_e32 v147, v148, v147
	v_div_scale_f32 v148, vcc, 1.0, v34, 1.0
	v_mul_f32_e32 v149, v148, v147
	v_fma_f32 v150, -v146, v149, v148
	v_fmac_f32_e32 v149, v150, v147
	v_fma_f32 v146, -v146, v149, v148
	v_div_fmas_f32 v146, v146, v147, v149
	v_div_fixup_f32 v34, v146, v34, 1.0
	v_pk_mul_f32 v[6:7], v[6:7], v[34:35] op_sel_hi:[1,0]
	v_pk_mul_f32 v[70:71], v[70:71], v[34:35] op_sel_hi:[1,0]
	v_pk_mul_f32 v[66:67], v[66:67], v[34:35] op_sel_hi:[1,0]
	v_pk_mul_f32 v[68:69], v[68:69], v[34:35] op_sel_hi:[1,0]
	v_pk_fma_f32 v[6:7], v[180:181], v[6:7], v[184:185]
	v_cvt_pk_fp8_f32 v146, v6, v7
	v_pk_fma_f32 v[70:71], v[182:183], v[70:71], v[186:187]
	v_lshl_add_u64 v[6:7], s[92:93], 0, v[2:3]
	v_pk_mul_f32 v[64:65], v[64:65], v[34:35] op_sel_hi:[1,0]
	v_cvt_pk_fp8_f32 v146, v70, v71 op_sel:[0,0,1]
	v_pk_mul_f32 v[62:63], v[62:63], v[34:35] op_sel_hi:[1,0]
	v_pk_mul_f32 v[58:59], v[58:59], v[34:35] op_sel_hi:[1,0]
	global_store_dword v[6:7], v146, off offset:-2048 sc0 sc1
	v_pk_mul_f32 v[60:61], v[60:61], v[34:35] op_sel_hi:[1,0]
	v_pk_mul_f32 v[56:57], v[56:57], v[34:35] op_sel_hi:[1,0]
	v_pk_mul_f32 v[54:55], v[54:55], v[34:35] op_sel_hi:[1,0]
	v_pk_mul_f32 v[32:33], v[32:33], v[34:35] op_sel_hi:[1,0]
	v_pk_fma_f32 v[66:67], v[188:189], v[66:67], v[192:193]
	v_pk_fma_f32 v[68:69], v[190:191], v[68:69], v[194:195]
	v_cvt_pk_fp8_f32 v70, v66, v67
	v_pk_mul_f32 v[52:53], v[52:53], v[34:35] op_sel_hi:[1,0]
	v_pk_mul_f32 v[30:31], v[30:31], v[34:35] op_sel_hi:[1,0]
	v_pk_mul_f32 v[28:29], v[28:29], v[34:35] op_sel_hi:[1,0]
	v_cvt_pk_fp8_f32 v70, v68, v69 op_sel:[0,0,1]
	v_pk_mul_f32 v[24:25], v[24:25], v[34:35] op_sel_hi:[1,0]
	v_pk_mul_f32 v[26:27], v[26:27], v[34:35] op_sel_hi:[1,0]
	global_store_dword v[6:7], v70, off offset:-1792 sc0 sc1
	v_pk_fma_f32 v[64:65], v[64:65], v[196:197], v[200:201]
	v_cvt_pk_fp8_f32 v66, v64, v65
	v_pk_fma_f32 v[62:63], v[62:63], v[198:199], v[202:203]
	s_nop 0
	v_cvt_pk_fp8_f32 v66, v62, v63 op_sel:[0,0,1]
	global_store_dword v[6:7], v66, off offset:-1536 sc0 sc1
	v_pk_fma_f32 v[58:59], v[58:59], v[204:205], v[208:209]
	v_cvt_pk_fp8_f32 v62, v58, v59
	v_pk_fma_f32 v[60:61], v[60:61], v[206:207], v[210:211]
	s_nop 0
	v_cvt_pk_fp8_f32 v62, v60, v61 op_sel:[0,0,1]
	global_store_dword v[6:7], v62, off offset:-1280 sc0 sc1
	v_pk_fma_f32 v[56:57], v[56:57], v[212:213], v[216:217]
	v_cvt_pk_fp8_f32 v58, v56, v57
	v_pk_fma_f32 v[54:55], v[54:55], v[214:215], v[218:219]
	s_nop 0
	v_cvt_pk_fp8_f32 v58, v54, v55 op_sel:[0,0,1]
	global_store_dword v[6:7], v58, off offset:-1024 sc0 sc1
	v_pk_fma_f32 v[32:33], v[32:33], v[220:221], v[224:225]
	v_cvt_pk_fp8_f32 v54, v32, v33
	v_pk_fma_f32 v[52:53], v[52:53], v[222:223], v[226:227]
	v_cvt_pk_fp8_f32 v54, v52, v53 op_sel:[0,0,1]
	global_store_dword v[6:7], v54, off offset:-768 sc0 sc1
	v_pk_fma_f32 v[30:31], v[30:31], v[228:229], v[232:233]
	s_nop 0
	v_cvt_pk_fp8_f32 v32, v30, v31
	v_pk_fma_f32 v[28:29], v[28:29], v[230:231], v[234:235]
	s_nop 0
	v_cvt_pk_fp8_f32 v32, v28, v29 op_sel:[0,0,1]
	global_store_dword v[6:7], v32, off offset:-512 sc0 sc1
	v_pk_fma_f32 v[24:25], v[24:25], v[236:237], v[240:241]
	v_cvt_pk_fp8_f32 v28, v24, v25
	v_pk_fma_f32 v[26:27], v[26:27], v[238:239], v[242:243]
	s_nop 0
	v_cvt_pk_fp8_f32 v28, v26, v27 op_sel:[0,0,1]
	global_store_dword v[6:7], v28, off offset:-256 sc0 sc1
	s_and_saveexec_b64 s[12:13], s[8:9]
	s_cbranch_execz .LBB0_708
	s_add_i32 s70, s37, -8
	s_add_u32 s68, s92, s14
	v_mul_f32_e32 v24, 0x3a000000, v145
	s_addc_u32 s69, s93, s15
	v_mov_b32_e32 v25, v34
	v_mov_b32_e32 v26, s70
	ds_write_b64 v26, v[24:25]
	global_store_dwordx2 v137, v[24:25], s[68:69]
.LBB0_708:
	s_or_b64 exec, exec, s[12:13]
	s_waitcnt vmcnt(23)
	v_lshlrev_b32_e32 v58, 16, v22
	v_and_b32_e32 v59, 0xffff0000, v22
	v_lshlrev_b32_e32 v56, 16, v23
	v_and_b32_e32 v57, 0xffff0000, v23
	v_add_f32_e32 v22, v58, v59
	v_add_f32_e32 v23, v56, v57
	s_waitcnt vmcnt(22)
	v_lshlrev_b32_e32 v52, 16, v20
	v_and_b32_e32 v53, 0xffff0000, v20
	v_lshlrev_b32_e32 v54, 16, v21
	v_and_b32_e32 v55, 0xffff0000, v21
	v_add_f32_e32 v22, v22, v23
	v_add_f32_e32 v20, v52, v53
	v_add_f32_e32 v21, v54, v55
	s_waitcnt vmcnt(21)
	v_lshlrev_b32_e32 v32, 16, v18
	v_and_b32_e32 v33, 0xffff0000, v18
	v_lshlrev_b32_e32 v30, 16, v19
	v_and_b32_e32 v31, 0xffff0000, v19
	v_add_f32_e32 v22, 0, v22
	v_add_f32_e32 v20, v20, v21
	v_add_f32_e32 v18, v32, v33
	v_add_f32_e32 v19, v30, v31
	v_add_f32_e32 v20, v22, v20
	v_add_f32_e32 v18, v18, v19
	s_waitcnt vmcnt(20)
	v_lshlrev_b32_e32 v26, 16, v16
	v_and_b32_e32 v27, 0xffff0000, v16
	v_lshlrev_b32_e32 v28, 16, v17
	v_and_b32_e32 v29, 0xffff0000, v17
	v_add_f32_e32 v18, v20, v18
	v_add_f32_e32 v16, v26, v27
	v_add_f32_e32 v17, v28, v29
	s_waitcnt vmcnt(19)
	v_lshlrev_b32_e32 v22, 16, v14
	v_and_b32_e32 v23, 0xffff0000, v14
	v_lshlrev_b32_e32 v20, 16, v15
	v_and_b32_e32 v21, 0xffff0000, v15
	v_add_f32_e32 v16, v16, v17
	v_add_f32_e32 v14, v22, v23
	v_add_f32_e32 v15, v20, v21
	v_add_f32_e32 v16, v18, v16
	v_add_f32_e32 v14, v14, v15
	v_add_f32_e32 v14, v16, v14
	s_waitcnt vmcnt(18)
	v_lshlrev_b32_e32 v16, 16, v12
	v_and_b32_e32 v17, 0xffff0000, v12
	v_lshlrev_b32_e32 v18, 16, v13
	v_and_b32_e32 v19, 0xffff0000, v13
	v_add_f32_e32 v12, v16, v17
	v_add_f32_e32 v13, v18, v19
	v_add_f32_e32 v12, v12, v13
	v_add_f32_e32 v24, v14, v12
	s_waitcnt vmcnt(17)
	v_lshlrev_b32_e32 v14, 16, v10
	v_and_b32_e32 v15, 0xffff0000, v10
	v_lshlrev_b32_e32 v12, 16, v11
	v_and_b32_e32 v13, 0xffff0000, v11
	v_add_f32_e32 v10, v14, v15
	v_add_f32_e32 v11, v12, v13
	v_add_f32_e32 v10, v10, v11
	v_add_f32_e32 v24, v24, v10
	s_waitcnt vmcnt(16)
	v_lshlrev_b32_e32 v10, 16, v8
	v_and_b32_e32 v11, 0xffff0000, v8
	v_lshlrev_b32_e32 v8, 16, v9
	v_and_b32_e32 v9, 0xffff0000, v9
	v_add_f32_e32 v25, v10, v11
	v_add_f32_e32 v34, v8, v9
	v_add_f32_e32 v25, v25, v34
	v_add_f32_e32 v24, v24, v25
	s_nop 1
	v_add_f32_dpp v24, v24, v24 quad_perm:[1,0,3,2] row_mask:0xf bank_mask:0xf bound_ctrl:1
	s_nop 1
	v_add_f32_dpp v24, v24, v24 quad_perm:[2,3,0,1] row_mask:0xf bank_mask:0xf bound_ctrl:1
	s_nop 1
	v_add_f32_dpp v24, v24, v24 row_half_mirror row_mask:0xf bank_mask:0xf bound_ctrl:1
	s_nop 1
	v_add_f32_dpp v24, v24, v24 row_mirror row_mask:0xf bank_mask:0xf bound_ctrl:1
	v_mov_b32_e32 v25, v24
	s_nop 1
	v_permlane16_swap_b32_e32 v24, v25
	v_add_f32_e32 v24, v24, v25
	v_mov_b32_e32 v25, v24
	s_nop 1
	v_permlane32_swap_b32_e32 v24, v25
	v_add_f32_e32 v25, v24, v25
	v_fmac_f32_e32 v57, 0xba000000, v25
	v_fmac_f32_e32 v59, 0xba000000, v25
	v_fmac_f32_e32 v56, 0xba000000, v25
	v_fmac_f32_e32 v58, 0xba000000, v25
	v_mul_f32_e32 v24, v59, v59
	v_mul_f32_e32 v34, v57, v57
	v_fmac_f32_e32 v24, v58, v58
	v_fmac_f32_e32 v34, v56, v56
	v_fmac_f32_e32 v55, 0xba000000, v25
	v_fmac_f32_e32 v53, 0xba000000, v25
	v_add_f32_e32 v24, v24, v34
	v_fmac_f32_e32 v54, 0xba000000, v25
	v_fmac_f32_e32 v52, 0xba000000, v25
	v_mul_f32_e32 v34, v53, v53
	v_mul_f32_e32 v60, v55, v55
	v_fmac_f32_e32 v34, v52, v52
	v_fmac_f32_e32 v60, v54, v54
	v_add_f32_e32 v34, v34, v60
	v_fmac_f32_e32 v31, 0xba000000, v25
	v_fmac_f32_e32 v33, 0xba000000, v25
	v_add_f32_e32 v24, v24, v34
	v_fmac_f32_e32 v30, 0xba000000, v25
	v_fmac_f32_e32 v32, 0xba000000, v25
	v_mul_f32_e32 v34, v33, v33
	v_mul_f32_e32 v60, v31, v31
	v_fmac_f32_e32 v34, v32, v32
	v_fmac_f32_e32 v60, v30, v30
	v_add_f32_e32 v34, v34, v60
	v_fmac_f32_e32 v29, 0xba000000, v25
	v_fmac_f32_e32 v27, 0xba000000, v25
	v_add_f32_e32 v24, v34, v24
	v_fmac_f32_e32 v28, 0xba000000, v25
	v_fmac_f32_e32 v26, 0xba000000, v25
	v_mul_f32_e32 v34, v27, v27
	v_mul_f32_e32 v60, v29, v29
	v_fmac_f32_e32 v34, v26, v26
	v_fmac_f32_e32 v60, v28, v28
	v_add_f32_e32 v34, v34, v60
	v_fmac_f32_e32 v21, 0xba000000, v25
	v_fmac_f32_e32 v23, 0xba000000, v25
	v_add_f32_e32 v24, v34, v24
	v_fmac_f32_e32 v20, 0xba000000, v25
	v_fmac_f32_e32 v22, 0xba000000, v25
	v_mul_f32_e32 v34, v23, v23
	v_mul_f32_e32 v60, v21, v21
	v_fmac_f32_e32 v34, v22, v22
	v_fmac_f32_e32 v60, v20, v20
	v_add_f32_e32 v34, v34, v60
	v_fmac_f32_e32 v19, 0xba000000, v25
	v_fmac_f32_e32 v17, 0xba000000, v25
	v_add_f32_e32 v24, v34, v24
	v_fmac_f32_e32 v18, 0xba000000, v25
	v_fmac_f32_e32 v16, 0xba000000, v25
	v_mul_f32_e32 v34, v17, v17
	v_mul_f32_e32 v60, v19, v19
	v_fmac_f32_e32 v34, v16, v16
	v_fmac_f32_e32 v60, v18, v18
	v_add_f32_e32 v34, v34, v60
	v_fmac_f32_e32 v13, 0xba000000, v25
	v_fmac_f32_e32 v15, 0xba000000, v25
	v_add_f32_e32 v24, v34, v24
	v_fmac_f32_e32 v12, 0xba000000, v25
	v_fmac_f32_e32 v14, 0xba000000, v25
	v_mul_f32_e32 v34, v15, v15
	v_mul_f32_e32 v60, v13, v13
	v_fmac_f32_e32 v34, v14, v14
	v_fmac_f32_e32 v60, v12, v12
	v_add_f32_e32 v34, v34, v60
	v_fmac_f32_e32 v9, 0xba000000, v25
	v_fmac_f32_e32 v11, 0xba000000, v25
	v_add_f32_e32 v24, v34, v24
	v_fmac_f32_e32 v8, 0xba000000, v25
	v_fmac_f32_e32 v10, 0xba000000, v25
	v_mul_f32_e32 v34, v11, v11
	v_mul_f32_e32 v60, v9, v9
	v_fmac_f32_e32 v34, v10, v10
	v_fmac_f32_e32 v60, v8, v8
	v_add_f32_e32 v34, v34, v60
	v_add_f32_e32 v24, v34, v24
	s_nop 1
	v_add_f32_dpp v24, v24, v24 quad_perm:[1,0,3,2] row_mask:0xf bank_mask:0xf bound_ctrl:1
	s_nop 1
	v_add_f32_dpp v24, v24, v24 quad_perm:[2,3,0,1] row_mask:0xf bank_mask:0xf bound_ctrl:1
	s_nop 1
	v_add_f32_dpp v24, v24, v24 row_half_mirror row_mask:0xf bank_mask:0xf bound_ctrl:1
	s_nop 1
	v_add_f32_dpp v24, v24, v24 row_mirror row_mask:0xf bank_mask:0xf bound_ctrl:1
	v_mov_b32_e32 v34, v24
	s_nop 1
	v_permlane16_swap_b32_e32 v24, v34
	v_add_f32_e32 v24, v24, v34
	v_mov_b32_e32 v34, v24
	s_nop 1
	v_permlane32_swap_b32_e32 v24, v34
	v_add_f32_e32 v24, v24, v34
	v_fmamk_f32 v24, v24, 0x3a000000, v135
	v_cmp_gt_f32_e32 vcc, s44, v24
	v_mul_f32_e32 v34, 0x4f800000, v24
	s_nop 0
	v_cndmask_b32_e32 v24, v24, v34, vcc
	v_sqrt_f32_e32 v34, v24
	s_nop 0
	v_add_u32_e32 v60, -1, v34
	v_fma_f32 v61, -v60, v34, v24
	v_cmp_ge_f32_e64 s[12:13], 0, v61
	v_add_u32_e32 v61, 1, v34
	s_nop 0
	v_cndmask_b32_e64 v60, v34, v60, s[12:13]
	v_fma_f32 v34, -v61, v34, v24
	v_cmp_lt_f32_e64 s[12:13], 0, v34
	s_nop 1
	v_cndmask_b32_e64 v34, v60, v61, s[12:13]
	v_mul_f32_e32 v60, 0x37800000, v34
	v_cndmask_b32_e32 v34, v34, v60, vcc
	v_cmp_class_f32_e32 vcc, v24, v136
	s_nop 1
	v_cndmask_b32_e32 v24, v34, v24, vcc
	v_div_scale_f32 v34, s[12:13], v24, v24, 1.0
	v_rcp_f32_e32 v60, v34
	s_nop 0
	v_fma_f32 v61, -v34, v60, 1.0
	v_fmac_f32_e32 v60, v61, v60
	v_div_scale_f32 v61, vcc, 1.0, v24, 1.0
	v_mul_f32_e32 v62, v61, v60
	v_fma_f32 v63, -v34, v62, v61
	v_fmac_f32_e32 v62, v63, v60
	v_fma_f32 v34, -v34, v62, v61
	v_div_fmas_f32 v34, v34, v60, v62
	v_div_fixup_f32 v24, v34, v24, 1.0
	v_pk_mul_f32 v[58:59], v[58:59], v[24:25] op_sel_hi:[1,0]
	v_pk_mul_f32 v[56:57], v[56:57], v[24:25] op_sel_hi:[1,0]
	v_pk_fma_f32 v[58:59], v[180:181], v[58:59], v[184:185]
	v_pk_fma_f32 v[56:57], v[182:183], v[56:57], v[186:187]
	v_cvt_pk_fp8_f32 v34, v58, v59
	v_pk_mul_f32 v[52:53], v[52:53], v[24:25] op_sel_hi:[1,0]
	v_pk_mul_f32 v[54:55], v[54:55], v[24:25] op_sel_hi:[1,0]
	v_pk_mul_f32 v[32:33], v[32:33], v[24:25] op_sel_hi:[1,0]
	v_cvt_pk_fp8_f32 v34, v56, v57 op_sel:[0,0,1]
	v_pk_mul_f32 v[30:31], v[30:31], v[24:25] op_sel_hi:[1,0]
	v_pk_mul_f32 v[26:27], v[26:27], v[24:25] op_sel_hi:[1,0]
	v_pk_mul_f32 v[28:29], v[28:29], v[24:25] op_sel_hi:[1,0]
	global_store_dword v[6:7], v34, off sc0 sc1
	v_pk_mul_f32 v[22:23], v[22:23], v[24:25] op_sel_hi:[1,0]
	v_pk_mul_f32 v[20:21], v[20:21], v[24:25] op_sel_hi:[1,0]
	v_pk_mul_f32 v[16:17], v[16:17], v[24:25] op_sel_hi:[1,0]
	v_pk_fma_f32 v[52:53], v[188:189], v[52:53], v[192:193]
	v_pk_fma_f32 v[54:55], v[190:191], v[54:55], v[194:195]
	v_cvt_pk_fp8_f32 v34, v52, v53
	v_pk_mul_f32 v[18:19], v[18:19], v[24:25] op_sel_hi:[1,0]
	v_pk_mul_f32 v[14:15], v[14:15], v[24:25] op_sel_hi:[1,0]
	v_pk_mul_f32 v[12:13], v[12:13], v[24:25] op_sel_hi:[1,0]
	v_cvt_pk_fp8_f32 v34, v54, v55 op_sel:[0,0,1]
	v_pk_mul_f32 v[10:11], v[10:11], v[24:25] op_sel_hi:[1,0]
	v_pk_mul_f32 v[8:9], v[8:9], v[24:25] op_sel_hi:[1,0]
	global_store_dword v[6:7], v34, off offset:256 sc0 sc1
	v_pk_fma_f32 v[32:33], v[32:33], v[196:197], v[200:201]
	s_nop 0
	v_cvt_pk_fp8_f32 v34, v32, v33
	v_pk_fma_f32 v[30:31], v[30:31], v[198:199], v[202:203]
	s_nop 0
	v_cvt_pk_fp8_f32 v34, v30, v31 op_sel:[0,0,1]
	global_store_dword v[6:7], v34, off offset:512 sc0 sc1
	v_pk_fma_f32 v[26:27], v[26:27], v[204:205], v[208:209]
	v_cvt_pk_fp8_f32 v30, v26, v27
	v_pk_fma_f32 v[28:29], v[28:29], v[206:207], v[210:211]
	s_nop 0
	v_cvt_pk_fp8_f32 v30, v28, v29 op_sel:[0,0,1]
	global_store_dword v[6:7], v30, off offset:768 sc0 sc1
	v_pk_fma_f32 v[22:23], v[22:23], v[212:213], v[216:217]
	v_cvt_pk_fp8_f32 v26, v22, v23
	v_pk_fma_f32 v[20:21], v[20:21], v[214:215], v[218:219]
	s_nop 0
	v_cvt_pk_fp8_f32 v26, v20, v21 op_sel:[0,0,1]
	global_store_dword v[6:7], v26, off offset:1024 sc0 sc1
	v_pk_fma_f32 v[16:17], v[16:17], v[220:221], v[224:225]
	v_cvt_pk_fp8_f32 v20, v16, v17
	v_pk_fma_f32 v[18:19], v[18:19], v[222:223], v[226:227]
	s_nop 0
	v_cvt_pk_fp8_f32 v20, v18, v19 op_sel:[0,0,1]
	global_store_dword v[6:7], v20, off offset:1280 sc0 sc1
	v_pk_fma_f32 v[14:15], v[14:15], v[228:229], v[232:233]
	v_cvt_pk_fp8_f32 v16, v14, v15
	v_pk_fma_f32 v[12:13], v[12:13], v[230:231], v[234:235]
	s_nop 0
	v_cvt_pk_fp8_f32 v16, v12, v13 op_sel:[0,0,1]
	global_store_dword v[6:7], v16, off offset:1536 sc0 sc1
	v_pk_fma_f32 v[10:11], v[10:11], v[236:237], v[240:241]
	v_cvt_pk_fp8_f32 v12, v10, v11
	v_pk_fma_f32 v[8:9], v[8:9], v[238:239], v[242:243]
	s_nop 0
	v_cvt_pk_fp8_f32 v12, v8, v9 op_sel:[0,0,1]
	global_store_dword v[6:7], v12, off offset:1792 sc0 sc1
	s_and_saveexec_b64 s[12:13], s[8:9]
	s_cbranch_execz .LBB0_705
	s_add_u32 s68, s92, s14
	v_mul_f32_e32 v6, 0x3a000000, v25
	s_addc_u32 s69, s93, s15
	v_mov_b32_e32 v7, v24
	v_mov_b32_e32 v8, s37
	ds_write_b64 v8, v[6:7]
	global_store_dwordx2 v137, v[6:7], s[68:69] offset:8
	s_branch .LBB0_705
